# attention QK^T K-fragment pipelining extended to the second peeled iteration of each flash loop and the importance loop
# speedup vs baseline: 1.0253x; 1.0037x over previous
; #define LAS __attribute__((address_space(3)))
; #define SBAR() __builtin_amdgcn_sched_barrier(0)
; template <int OFF> __device__ __forceinline__ s16x4 tr_read(int vb) { s16x4 r; asm volatile("ds_read_b64_tr_b16 %0, %1 offset:%2" : "=&v"(r) : "v"(vb), "i"(OFF) : "memory"); return r; }
; __device__ __forceinline__ void qkt(f32x16& p0, f32x16& p1, const LAS char* Ks, const bf16x8 (&qr)[8], int r32, int hi) {
;     p0 = f32x16{}; p1 = f32x16{};
; #pragma unroll
;     for (int d0 = 0; d0 < 8; ++d0) { const int cb = (d0 * 16 + hi * 8) * 2;
;         const bf16x8 b0 = *(const LAS bf16x8*)(Ks + KSWZ(r32, cb));
;         const bf16x8 b1 = *(const LAS bf16x8*)(Ks + KSWZ(32 + r32, cb));
;         p0 = __builtin_amdgcn_mfma_f32_32x32x16_bf16(b0, qr[d0], p0, 0, 0, 0);
;         p1 = __builtin_amdgcn_mfma_f32_32x32x16_bf16(b1, qr[d0], p1, 0, 0, 0);
;         if (d0 == 3) SBAR(); }
; }
; template <int D0> __device__ __forceinline__ void pv_one(f32x16& od, int vb, bf16x8 pa0, bf16x8 pa1, bf16x8 pa2, bf16x8 pa3) {
;     const s16x4 l0 = tr_read<v_rd_off(D0, 0, 0)>(vb), h0 = tr_read<v_rd_off(D0, 0, 1)>(vb), l1 = tr_read<v_rd_off(D0, 1, 0)>(vb), h1 = tr_read<v_rd_off(D0, 1, 1)>(vb);
;     const s16x4 l2 = tr_read<v_rd_off(D0, 2, 0)>(vb), h2 = tr_read<v_rd_off(D0, 2, 1)>(vb), l3 = tr_read<v_rd_off(D0, 3, 0)>(vb), h3 = tr_read<v_rd_off(D0, 3, 1)>(vb);
;     asm volatile("s_waitcnt lgkmcnt(0)" ::: "memory"); SBAR();
;     ...
;     od = __builtin_amdgcn_mfma_f32_32x32x16_bf16(pa0, PK(l0, h0), od, 0, 0, 0);
;     od = __builtin_amdgcn_mfma_f32_32x32x16_bf16(pa1, PK(l1, h1), od, 0, 0, 0);
;     od = __builtin_amdgcn_mfma_f32_32x32x16_bf16(pa2, PK(l2, h2), od, 0, 0, 0);
;     od = __builtin_amdgcn_mfma_f32_32x32x16_bf16(pa3, PK(l3, h3), od, 0, 0, 0);
;     ...
; }
.LBB0_578:
	s_barrier
	v_add_f32_e32 v2, v2, v20
	v_add_f32_e32 v2, v52, v2
	s_andn2_b64 vcc, exec, s[12:13]
	s_mov_b32 s26, 1
	s_cbranch_vccnz .LBB0_585
	v_readlane_b32 s12, v245, 31
	v_add_u32_e32 v144, 0xc000, v148
	s_nop 0
	v_mov_b32_e32 v20, s12
	ds_read_b32 v20, v20
	ds_read_b64_tr_b16 v[36:37], v165 offset:0
	ds_read_b64_tr_b16 v[38:39], v165 offset:0x800
	ds_read_b64_tr_b16 v[40:41], v165 offset:0x1000
	ds_read_b64_tr_b16 v[42:43], v165 offset:0x1800
	ds_read_b64_tr_b16 v[44:45], v165 offset:0x2000
	ds_read_b64_tr_b16 v[46:47], v165 offset:0x2800
	ds_read_b64_tr_b16 v[48:49], v165 offset:0x3000
	ds_read_b64_tr_b16 v[50:51], v165 offset:0x3800
	s_waitcnt lgkmcnt(0)
	s_waitcnt lgkmcnt(0)
	v_readfirstlane_b32 s26, v20
	v_mfma_f32_32x32x16_bf16 v[20:35], v[72:75], v[36:39], v[4:19]
	v_add_u32_e32 v247, v144, v149
	ds_read_b128 v[212:215], v247 offset:16384
	ds_read_b64_tr_b16 v[52:53], v165 offset:0x200
	ds_read_b64_tr_b16 v[54:55], v165 offset:0xa00
	ds_read_b64_tr_b16 v[56:57], v165 offset:0x1200
	ds_read_b64_tr_b16 v[58:59], v165 offset:0x1a00
	ds_read_b64_tr_b16 v[60:61], v165 offset:0x2200
	ds_read_b64_tr_b16 v[62:63], v165 offset:0x2a00
	ds_read_b64_tr_b16 v[64:65], v165 offset:0x3200
	v_mfma_f32_32x32x16_bf16 v[20:35], v[76:79], v[40:43], v[20:35]
	ds_read_b128 v[216:219], v247 offset:24576
	ds_read_b64_tr_b16 v[66:67], v165 offset:0x3a00
	s_waitcnt lgkmcnt(0)
	v_mfma_f32_32x32x16_bf16 v[20:35], v[80:83], v[44:47], v[20:35]
	v_add_u32_e32 v247, v144, v150
	ds_read_b128 v[220:223], v247 offset:16384
	v_mfma_f32_32x32x16_bf16 v[20:35], v[68:71], v[48:51], v[20:35]
	ds_read_b128 v[224:227], v247 offset:24576
	v_mfma_f32_32x32x16_bf16 v[36:51], v[72:75], v[52:55], v[4:19]
	v_add_u32_e32 v247, v144, v151
	ds_read_b128 v[228:231], v247 offset:16384
	ds_read_b64_tr_b16 v[84:85], v165 offset:0x400
	ds_read_b64_tr_b16 v[86:87], v165 offset:0xc00
	ds_read_b64_tr_b16 v[88:89], v165 offset:0x1400
	ds_read_b64_tr_b16 v[90:91], v165 offset:0x1c00
	ds_read_b64_tr_b16 v[92:93], v165 offset:0x2400
	ds_read_b64_tr_b16 v[94:95], v165 offset:0x2c00
	ds_read_b64_tr_b16 v[96:97], v165 offset:0x3400
	v_mfma_f32_32x32x16_bf16 v[36:51], v[76:79], v[56:59], v[36:51]
	ds_read_b128 v[232:235], v247 offset:24576
	ds_read_b64_tr_b16 v[98:99], v165 offset:0x3c00
	s_waitcnt lgkmcnt(0)
	v_mfma_f32_32x32x16_bf16 v[36:51], v[80:83], v[60:63], v[36:51]
	v_add_u32_e32 v247, v144, v167
	ds_read_b128 v[236:239], v247 offset:16384
	v_mfma_f32_32x32x16_bf16 v[36:51], v[68:71], v[64:67], v[36:51]
	ds_read_b128 v[240:243], v247 offset:24576
	v_mfma_f32_32x32x16_bf16 v[52:67], v[72:75], v[84:87], v[4:19]
	ds_read_b64_tr_b16 v[84:85], v165 offset:0x600
	ds_read_b64_tr_b16 v[86:87], v165 offset:0xe00
	v_mfma_f32_32x32x16_bf16 v[52:67], v[76:79], v[88:91], v[52:67]
	ds_read_b64_tr_b16 v[88:89], v165 offset:0x1600
	ds_read_b64_tr_b16 v[90:91], v165 offset:0x1e00
	v_mfma_f32_32x32x16_bf16 v[52:67], v[80:83], v[92:95], v[52:67]
	ds_read_b64_tr_b16 v[92:93], v165 offset:0x2600
	ds_read_b64_tr_b16 v[94:95], v165 offset:0x2e00
	v_mfma_f32_32x32x16_bf16 v[52:67], v[68:71], v[96:99], v[52:67]
	ds_read_b64_tr_b16 v[96:97], v165 offset:0x3600
	ds_read_b64_tr_b16 v[98:99], v165 offset:0x3e00
	s_waitcnt lgkmcnt(0)
	v_mfma_f32_32x32x16_bf16 v[4:19], v[72:75], v[84:87], v[4:19]
	v_mfma_f32_32x32x16_bf16 v[4:19], v[76:79], v[88:91], v[4:19]
	v_mfma_f32_32x32x16_bf16 v[4:19], v[80:83], v[92:95], v[4:19]
	v_mfma_f32_32x32x16_bf16 v[4:19], v[68:71], v[96:99], v[4:19]
	v_mfma_f32_32x32x16_bf16 v[68:83], v[212:215], v[124:127], 0
	v_add_u32_e32 v247, v144, v169
	ds_read_b128 v[212:215], v247 offset:16384
	v_mfma_f32_32x32x16_bf16 v[84:99], v[216:219], v[124:127], 0
	ds_read_b128 v[216:219], v247 offset:24576
	v_mfma_f32_32x32x16_bf16 v[68:83], v[220:223], v[100:103], v[68:83]
	v_add_u32_e32 v247, v144, v176
	ds_read_b128 v[220:223], v247 offset:16384
	v_mfma_f32_32x32x16_bf16 v[84:99], v[224:227], v[100:103], v[84:99]
	ds_read_b128 v[224:227], v247 offset:24576
	v_mfma_f32_32x32x16_bf16 v[68:83], v[228:231], v[104:107], v[68:83]
	v_add_u32_e32 v247, v144, v177
	ds_read_b128 v[228:231], v247 offset:16384
	v_mfma_f32_32x32x16_bf16 v[84:99], v[232:235], v[104:107], v[84:99]
	ds_read_b128 v[232:235], v247 offset:24576
	v_mfma_f32_32x32x16_bf16 v[68:83], v[236:239], v[108:111], v[68:83]
	v_add_u32_e32 v247, v144, v178
	ds_read_b128 v[236:239], v247 offset:16384
	v_mfma_f32_32x32x16_bf16 v[84:99], v[240:243], v[108:111], v[84:99]
	ds_read_b128 v[240:243], v247 offset:24576
	s_waitcnt lgkmcnt(7)
	v_mfma_f32_32x32x16_bf16 v[68:83], v[212:215], v[112:115], v[68:83]
	s_waitcnt lgkmcnt(6)
	v_mfma_f32_32x32x16_bf16 v[84:99], v[216:219], v[112:115], v[84:99]
	s_waitcnt lgkmcnt(5)
	v_mfma_f32_32x32x16_bf16 v[68:83], v[220:223], v[116:119], v[68:83]
	s_waitcnt lgkmcnt(4)
	v_mfma_f32_32x32x16_bf16 v[84:99], v[224:227], v[116:119], v[84:99]
	s_waitcnt lgkmcnt(3)
	v_mfma_f32_32x32x16_bf16 v[68:83], v[228:231], v[120:123], v[68:83]
	s_waitcnt lgkmcnt(2)
	v_mfma_f32_32x32x16_bf16 v[84:99], v[232:235], v[120:123], v[84:99]
	s_waitcnt lgkmcnt(1)
	v_mfma_f32_32x32x16_bf16 v[68:83], v[236:239], v[128:131], v[68:83]
	s_waitcnt lgkmcnt(0)
	s_andn2_b64 vcc, exec, s[16:17]
	v_cndmask_b32_e64 v144, 0, 1, s[16:17]
	v_cmp_ne_u32_e64 s[12:13], 1, v144
	v_mfma_f32_32x32x16_bf16 v[84:99], v[240:243], v[128:131], v[84:99]
	s_cbranch_vccnz .LBB0_581
	s_waitcnt vmcnt(0)

; #define LAS __attribute__((address_space(3)))
; #define SBAR() __builtin_amdgcn_sched_barrier(0)
; __device__ __forceinline__ void qkt(f32x16& p0, f32x16& p1, const LAS char* Ks, const bf16x8 (&qr)[8], int r32, int hi) {
;     p0 = f32x16{}; p1 = f32x16{};
; #pragma unroll
;     for (int d0 = 0; d0 < 8; ++d0) { const int cb = (d0 * 16 + hi * 8) * 2;
;         const bf16x8 b0 = *(const LAS bf16x8*)(Ks + KSWZ(r32, cb));
;         const bf16x8 b1 = *(const LAS bf16x8*)(Ks + KSWZ(32 + r32, cb));
;         p0 = __builtin_amdgcn_mfma_f32_32x32x16_bf16(b0, qr[d0], p0, 0, 0, 0);
;         p1 = __builtin_amdgcn_mfma_f32_32x32x16_bf16(b1, qr[d0], p1, 0, 0, 0);
;         if (d0 == 3) SBAR(); }
; }
; template <int MODE>
; __device__ __forceinline__ void bias_mask(f32x16& p0, f32x16& p1, int b, int t, int hi, float slope2, bool selbit) {
;     const float base = (MODE == 0) ? (float)(t - 31 - 1024 * b - 64 * hi) : (float)(t - 64 * b - 4 * hi);
;     const float nb = -slope2 * base;
; #pragma unroll
;     for (int r = 0; r < 16; ++r) {
;         const int c0 = (r & 3) + 8 * (r >> 2), c1 = 32 + c0;
;         const float k0 = (MODE == 0) ? 16.f * c0 : (float)c0, k1 = (MODE == 0) ? 16.f * c1 : (float)c1;
;         const float d0 = base - k0, d1 = base - k1;
;         bool v0 = d0 >= 0.f, v1 = d1 >= 0.f;
;         if (MODE == 1) { v0 = v0 && selbit; v1 = v1 && selbit; }
;         if (MODE == 2) { v0 = v0 && (d0 < 512.f); v1 = v1 && (d1 < 512.f); }
;         const float s0 = p0[r] + fmaf(slope2, k0, nb), s1 = p1[r] + fmaf(slope2, k1, nb);
;         p0[r] = v0 ? s0 : -__builtin_inff(); p1[r] = v1 ? s1 : -__builtin_inff();
;     }
.LBB0_629:
	s_and_b32 s10, s12, 0x4000
	v_add_u32_e32 v246, s10, v43
	v_add_u32_e32 v247, v246, v44
	ds_read_b128 v[212:215], v247 offset:49152
	ds_read_b128 v[216:219], v247 offset:57344
	v_add_u32_e32 v247, v246, v45
	ds_read_b128 v[220:223], v247 offset:49152
	ds_read_b128 v[224:227], v247 offset:57344
	v_add_u32_e32 v247, v246, v46
	ds_read_b128 v[228:231], v247 offset:49152
	ds_read_b128 v[232:235], v247 offset:57344
	v_add_u32_e32 v247, v246, v47
	ds_read_b128 v[236:239], v247 offset:49152
	ds_read_b128 v[240:243], v247 offset:57344
	s_waitcnt lgkmcnt(7)
	v_mfma_f32_32x32x16_bf16 v[4:19], v[212:215], v[124:127], 0
	v_add_u32_e32 v247, v246, v48
	ds_read_b128 v[212:215], v247 offset:49152
	s_waitcnt lgkmcnt(7)
	v_mfma_f32_32x32x16_bf16 v[20:35], v[216:219], v[124:127], 0
	ds_read_b128 v[216:219], v247 offset:57344
	s_waitcnt lgkmcnt(7)
	v_mfma_f32_32x32x16_bf16 v[4:19], v[220:223], v[100:103], v[4:19]
	v_add_u32_e32 v247, v246, v49
	ds_read_b128 v[220:223], v247 offset:49152
	s_waitcnt lgkmcnt(7)
	v_mfma_f32_32x32x16_bf16 v[20:35], v[224:227], v[100:103], v[20:35]
	ds_read_b128 v[224:227], v247 offset:57344
	s_waitcnt lgkmcnt(7)
	v_mfma_f32_32x32x16_bf16 v[4:19], v[228:231], v[104:107], v[4:19]
	v_add_u32_e32 v247, v246, v50
	ds_read_b128 v[228:231], v247 offset:49152
	s_waitcnt lgkmcnt(7)
	v_mfma_f32_32x32x16_bf16 v[20:35], v[232:235], v[104:107], v[20:35]
	ds_read_b128 v[232:235], v247 offset:57344
	s_waitcnt lgkmcnt(7)
	v_mfma_f32_32x32x16_bf16 v[4:19], v[236:239], v[108:111], v[4:19]
	v_add_u32_e32 v247, v246, v51
	ds_read_b128 v[236:239], v247 offset:49152
	s_waitcnt lgkmcnt(7)
	v_mfma_f32_32x32x16_bf16 v[20:35], v[240:243], v[108:111], v[20:35]
	ds_read_b128 v[240:243], v247 offset:57344
	s_waitcnt lgkmcnt(7)
	v_mfma_f32_32x32x16_bf16 v[4:19], v[212:215], v[112:115], v[4:19]
	s_waitcnt lgkmcnt(6)
	v_mfma_f32_32x32x16_bf16 v[20:35], v[216:219], v[112:115], v[20:35]
	s_waitcnt lgkmcnt(5)
	v_mfma_f32_32x32x16_bf16 v[4:19], v[220:223], v[116:119], v[4:19]
	s_waitcnt lgkmcnt(4)
	v_mfma_f32_32x32x16_bf16 v[20:35], v[224:227], v[116:119], v[20:35]
	s_waitcnt lgkmcnt(3)
	v_mfma_f32_32x32x16_bf16 v[4:19], v[228:231], v[120:123], v[4:19]
	s_waitcnt lgkmcnt(2)
	v_mfma_f32_32x32x16_bf16 v[20:35], v[232:235], v[120:123], v[20:35]
	s_waitcnt lgkmcnt(1)
	v_mfma_f32_32x32x16_bf16 v[4:19], v[236:239], v[128:131], v[4:19]
	s_waitcnt lgkmcnt(0)
	v_cmp_lt_i32_e64 s[10:11], -1, v52
	v_cvt_f32_i32_e32 v54, v52
	v_mul_f32_e64 v54, -v134, v54
	v_fma_f32 v55, 0, v134, v54
	s_nop 8
	v_add_f32_e32 v4, v55, v4
	v_mfma_f32_32x32x16_bf16 v[20:35], v[240:243], v[128:131], v[20:35]
	v_fmamk_f32 v55, v134, 0x44000000, v54
	v_cndmask_b32_e64 v4, v161, v4, s[10:11]
	v_cmp_lt_i32_e64 s[10:11], s33, v52
	v_sub_f32_e32 v4, v4, v175
	s_nop 7
	v_add_f32_e32 v20, v55, v20
	v_fmamk_f32 v55, v134, 0x41800000, v54
	v_cndmask_b32_e64 v20, v161, v20, s[10:11]
	v_add_f32_e32 v5, v55, v5
	v_fmamk_f32 v55, v134, 0x44040000, v54
	v_cmp_lt_i32_e64 s[10:11], 15, v52
	v_add_f32_e32 v21, v55, v21
	s_nop 0
	v_cndmask_b32_e64 v55, v161, v5, s[10:11]
	v_cmp_lt_i32_e64 s[10:11], s89, v52
	v_fmamk_f32 v5, v134, 0x42000000, v54
	v_add_f32_e32 v5, v5, v6
	v_cndmask_b32_e64 v21, v161, v21, s[10:11]
	v_fmamk_f32 v6, v134, 0x44080000, v54
	v_cmp_lt_i32_e64 s[10:11], 31, v52
	v_add_f32_e32 v6, v6, v22
	s_nop 0
	v_cndmask_b32_e64 v22, v161, v5, s[10:11]
	v_cmp_lt_i32_e64 s[10:11], s88, v52
	v_fmamk_f32 v5, v134, 0x42400000, v54
	v_add_f32_e32 v5, v5, v7
	v_cndmask_b32_e64 v56, v161, v6, s[10:11]
	v_fmamk_f32 v6, v134, 0x440c0000, v54
	v_cmp_lt_i32_e64 s[10:11], 47, v52
	v_add_f32_e32 v6, v6, v23
	s_nop 0
	v_cndmask_b32_e64 v23, v161, v5, s[10:11]
	v_cmp_lt_i32_e64 s[10:11], s93, v52
	v_fmamk_f32 v5, v134, 0x43000000, v54
	v_add_f32_e32 v5, v5, v8
	v_cndmask_b32_e64 v57, v161, v6, s[10:11]
	v_fmamk_f32 v6, v134, 0x44200000, v54
	v_cmp_lt_i32_e64 s[10:11], s36, v52
	v_add_f32_e32 v6, v6, v24
	s_nop 0
	v_cndmask_b32_e64 v24, v161, v5, s[10:11]
	v_cmp_lt_i32_e64 s[10:11], s92, v52
	v_fmamk_f32 v5, v134, 0x43100000, v54
	v_add_f32_e32 v5, v5, v9
	v_cndmask_b32_e64 v58, v161, v6, s[10:11]
	v_fmamk_f32 v6, v134, 0x44240000, v54
	v_cmp_lt_i32_e64 s[10:11], s66, v52
	v_add_f32_e32 v6, v6, v25
	s_nop 0
	v_cndmask_b32_e64 v25, v161, v5, s[10:11]
	v_cmp_lt_i32_e64 s[10:11], s87, v52
	v_fmamk_f32 v5, v134, 0x43200000, v54
	v_add_f32_e32 v5, v5, v10
	v_cndmask_b32_e64 v59, v161, v6, s[10:11]
	v_fmamk_f32 v6, v134, 0x44280000, v54
	v_cmp_lt_i32_e64 s[10:11], s77, v52
	v_add_f32_e32 v6, v6, v26
	s_nop 0
	v_cndmask_b32_e64 v60, v161, v5, s[10:11]
	v_cmp_lt_i32_e64 s[10:11], s86, v52
	v_fmamk_f32 v5, v134, 0x43300000, v54
	v_add_f32_e32 v5, v5, v11
	v_cndmask_b32_e64 v61, v161, v6, s[10:11]
	v_fmamk_f32 v6, v134, 0x442c0000, v54
	v_cmp_lt_i32_e64 s[10:11], s76, v52
	v_add_f32_e32 v6, v6, v27
	s_nop 0
	v_cndmask_b32_e64 v62, v161, v5, s[10:11]
	v_cmp_lt_i32_e64 s[10:11], s0, v52
	v_fmamk_f32 v5, v134, 0x43800000, v54
	v_add_f32_e32 v5, v5, v12
	v_cndmask_b32_e64 v63, v161, v6, s[10:11]
	v_fmamk_f32 v6, v134, 0x44400000, v54
	v_cmp_lt_i32_e64 s[10:11], s5, v52
	v_add_f32_e32 v6, v6, v28
	s_nop 0
	v_cndmask_b32_e64 v64, v161, v5, s[10:11]
	v_cmp_lt_i32_e64 s[10:11], s81, v52
	v_fmamk_f32 v5, v134, 0x43880000, v54
	v_add_f32_e32 v5, v5, v13
	v_cndmask_b32_e64 v65, v161, v6, s[10:11]
	v_fmamk_f32 v6, v134, 0x44440000, v54
	v_cmp_lt_i32_e64 s[10:11], s4, v52
	v_add_f32_e32 v6, v6, v29
	s_nop 0
	v_cndmask_b32_e64 v66, v161, v5, s[10:11]
	v_cmp_lt_i32_e64 s[10:11], s80, v52
	v_fmamk_f32 v5, v134, 0x43900000, v54
	v_add_f32_e32 v5, v5, v14
	v_cndmask_b32_e64 v67, v161, v6, s[10:11]
	v_fmamk_f32 v6, v134, 0x44480000, v54
; template <int MODE>
; __device__ __forceinline__ void bias_mask(f32x16& p0, f32x16& p1, int b, int t, int hi, float slope2, bool selbit) {
;     const float base = (MODE == 0) ? (float)(t - 31 - 1024 * b - 64 * hi) : (float)(t - 64 * b - 4 * hi);
;     const float nb = -slope2 * base;
; #pragma unroll
;     for (int r = 0; r < 16; ++r) {
;         const int c0 = (r & 3) + 8 * (r >> 2), c1 = 32 + c0;
;         const float k0 = (MODE == 0) ? 16.f * c0 : (float)c0, k1 = (MODE == 0) ? 16.f * c1 : (float)c1;
;         const float d0 = base - k0, d1 = base - k1;
;         bool v0 = d0 >= 0.f, v1 = d1 >= 0.f;
;         if (MODE == 1) { v0 = v0 && selbit; v1 = v1 && selbit; }
;         if (MODE == 2) { v0 = v0 && (d0 < 512.f); v1 = v1 && (d1 < 512.f); }
;         const float s0 = p0[r] + fmaf(slope2, k0, nb), s1 = p1[r] + fmaf(slope2, k1, nb);
;         p0[r] = v0 ? s0 : -__builtin_inff(); p1[r] = v1 ? s1 : -__builtin_inff();
;     }
; __device__ __forceinline__ void attn_unit(const Frame& F, unsigned char* ws, int g, int qt) {
;     ...
;         for (int r = 0; r < 16; ++r) { float v0 = __builtin_amdgcn_exp2f(p0[r] - m_c) * inv_lc, v1 = __builtin_amdgcn_exp2f(p1[r] - m_c) * inv_lc;
;             v0 += __int_as_float(__builtin_amdgcn_update_dpp(0, __float_as_int(v0), 0x128, 0xf, 0xf, false)); v1 += __int_as_float(__builtin_amdgcn_update_dpp(0, __float_as_int(v1), 0x128, 0xf, 0xf, false));
;             { auto q0 = __builtin_amdgcn_permlane16_swap(__float_as_uint(v0), __float_as_uint(v0), false, false); v0 = __uint_as_float(q0[0]) + __uint_as_float(q0[1]); }
;             { auto q1 = __builtin_amdgcn_permlane16_swap(__float_as_uint(v1), __float_as_uint(v1), false, false); v1 = __uint_as_float(q1[0]) + __uint_as_float(q1[1]); }
;             p0[r] = v0; p1[r] = v1; }
	v_cmp_lt_i32_e64 s[10:11], s73, v52
	v_add_f32_e32 v6, v6, v30
	s_nop 0
	v_cndmask_b32_e64 v68, v161, v5, s[10:11]
	v_cmp_lt_i32_e64 s[10:11], s79, v52
	v_fmamk_f32 v5, v134, 0x43980000, v54
	v_add_f32_e32 v5, v5, v15
	v_cndmask_b32_e64 v69, v161, v6, s[10:11]
	v_fmamk_f32 v6, v134, 0x444c0000, v54
	v_cmp_lt_i32_e64 s[10:11], s74, v52
	v_add_f32_e32 v6, v6, v31
	s_nop 0
	v_cndmask_b32_e64 v71, v161, v5, s[10:11]
	v_cmp_lt_i32_e64 s[10:11], s78, v52
	v_fmamk_f32 v5, v134, 0x43c00000, v54
	v_add_f32_e32 v5, v5, v16
	v_cndmask_b32_e64 v72, v161, v6, s[10:11]
	v_fmamk_f32 v6, v134, 0x44600000, v54
	v_cmp_lt_i32_e64 s[10:11], s26, v52
	v_add_f32_e32 v6, v6, v32
	s_nop 0
	v_cndmask_b32_e64 v73, v161, v5, s[10:11]
	v_cmp_lt_i32_e64 s[10:11], s71, v52
	v_fmamk_f32 v5, v134, 0x43c80000, v54
	v_add_f32_e32 v5, v5, v17
	v_cndmask_b32_e64 v74, v161, v6, s[10:11]
	v_fmamk_f32 v6, v134, 0x44640000, v54
	v_cmp_lt_i32_e64 s[10:11], s27, v52
	v_add_f32_e32 v6, v6, v33
	s_nop 0
	v_cndmask_b32_e64 v75, v161, v5, s[10:11]
	v_cmp_lt_i32_e64 s[10:11], s70, v52
	v_fmamk_f32 v5, v134, 0x43d00000, v54
	v_add_f32_e32 v5, v5, v18
	v_cndmask_b32_e64 v76, v161, v6, s[10:11]
	v_fmamk_f32 v6, v134, 0x44680000, v54
	v_cmp_lt_i32_e64 s[10:11], s28, v52
	v_add_f32_e32 v6, v6, v34
	v_sub_f32_e32 v75, v75, v175
	v_cndmask_b32_e64 v79, v161, v5, s[10:11]
	v_cmp_lt_i32_e64 s[10:11], s69, v52
	v_fmamk_f32 v5, v134, 0x43d80000, v54
	v_add_f32_e32 v5, v5, v19
	v_cndmask_b32_e64 v80, v161, v6, s[10:11]
	v_cmp_lt_i32_e64 s[10:11], s37, v52
	v_fmac_f32_e32 v54, 0x446c0000, v134
	v_add_f32_e32 v6, v54, v35
	v_cndmask_b32_e64 v83, v161, v5, s[10:11]
	v_exp_f32_e32 v5, v4
	v_sub_f32_e32 v4, v20, v175
	v_exp_f32_e32 v7, v4
	v_cmp_lt_i32_e64 s[10:11], s68, v52
	v_mov_b32_e32 v4, 0
	v_sub_f32_e32 v79, v79, v175
	v_cndmask_b32_e64 v84, v161, v6, s[10:11]
	v_mul_f32_e32 v6, v70, v5
	v_mul_f32_e32 v8, v70, v7
	v_sub_f32_e32 v83, v83, v175
	v_mov_b32_dpp v4, v6 row_ror:8 row_mask:0xf bank_mask:0xf
	v_fmac_f32_e32 v4, v70, v5
	v_mov_b32_e32 v5, 0
	v_mov_b32_e32 v6, v4
	s_nop 1
	v_permlane16_swap_b32_e32 v4, v6
	v_mov_b32_dpp v5, v8 row_ror:8 row_mask:0xf bank_mask:0xf
	v_sub_f32_e32 v8, v55, v175
	v_exp_f32_e32 v9, v8
	v_sub_f32_e32 v8, v21, v175
	v_exp_f32_e32 v10, v8
	v_mov_b32_e32 v8, 0
	v_mul_f32_e32 v11, v70, v9
	v_fmac_f32_e32 v5, v70, v7
	v_mul_f32_e32 v12, v70, v10
	v_mov_b32_dpp v8, v11 row_ror:8 row_mask:0xf bank_mask:0xf
	v_fmac_f32_e32 v8, v70, v9
	v_mov_b32_e32 v9, 0
	v_mov_b32_e32 v7, v5
	s_nop 1
	v_permlane16_swap_b32_e32 v5, v7
	v_mov_b32_dpp v9, v12 row_ror:8 row_mask:0xf bank_mask:0xf
	v_sub_f32_e32 v12, v22, v175
	v_exp_f32_e32 v13, v12
	v_sub_f32_e32 v12, v56, v175
	v_exp_f32_e32 v14, v12
	v_mov_b32_e32 v12, 0
	v_mul_f32_e32 v15, v70, v13
	v_fmac_f32_e32 v9, v70, v10
	v_mul_f32_e32 v16, v70, v14
	v_mov_b32_dpp v12, v15 row_ror:8 row_mask:0xf bank_mask:0xf
	v_fmac_f32_e32 v12, v70, v13
	v_mov_b32_e32 v13, 0
	v_mov_b32_e32 v10, v8
	v_mov_b32_e32 v11, v9
	v_mov_b32_dpp v13, v16 row_ror:8 row_mask:0xf bank_mask:0xf
	v_sub_f32_e32 v16, v23, v175
	v_exp_f32_e32 v17, v16
	v_sub_f32_e32 v16, v57, v175
	v_exp_f32_e32 v18, v16
	v_mov_b32_e32 v16, 0
	v_mul_f32_e32 v19, v70, v17
	v_fmac_f32_e32 v13, v70, v14
	v_mul_f32_e32 v20, v70, v18
	v_mov_b32_dpp v16, v19 row_ror:8 row_mask:0xf bank_mask:0xf
	v_fmac_f32_e32 v16, v70, v17
	v_mov_b32_e32 v17, 0
	v_mov_b32_e32 v14, v12
	v_mov_b32_e32 v15, v13
	v_mov_b32_dpp v17, v20 row_ror:8 row_mask:0xf bank_mask:0xf
	v_sub_f32_e32 v20, v24, v175
	v_exp_f32_e32 v21, v20
	v_sub_f32_e32 v20, v58, v175
	v_exp_f32_e32 v22, v20
	v_mov_b32_e32 v20, 0
	v_mul_f32_e32 v23, v70, v21
	v_fmac_f32_e32 v17, v70, v18
	v_mul_f32_e32 v24, v70, v22
	v_mov_b32_dpp v20, v23 row_ror:8 row_mask:0xf bank_mask:0xf
	v_fmac_f32_e32 v20, v70, v21
	v_mov_b32_e32 v21, 0
	v_mov_b32_e32 v18, v16
	v_mov_b32_e32 v19, v17
	v_mov_b32_dpp v21, v24 row_ror:8 row_mask:0xf bank_mask:0xf
	v_sub_f32_e32 v24, v25, v175
	v_exp_f32_e32 v25, v24
	v_sub_f32_e32 v24, v59, v175
	v_exp_f32_e32 v26, v24
	v_mov_b32_e32 v24, 0
	v_mul_f32_e32 v27, v70, v25
	v_fmac_f32_e32 v21, v70, v22
	v_mul_f32_e32 v28, v70, v26
	v_mov_b32_dpp v24, v27 row_ror:8 row_mask:0xf bank_mask:0xf
	v_fmac_f32_e32 v24, v70, v25
	v_mov_b32_e32 v25, 0
	v_mov_b32_e32 v22, v20
	v_mov_b32_e32 v23, v21
	v_mov_b32_dpp v25, v28 row_ror:8 row_mask:0xf bank_mask:0xf
	v_sub_f32_e32 v28, v60, v175
	v_exp_f32_e32 v29, v28
	v_sub_f32_e32 v28, v61, v175
	v_exp_f32_e32 v30, v28
	v_mov_b32_e32 v28, 0
	v_mul_f32_e32 v31, v70, v29
	v_fmac_f32_e32 v25, v70, v26
	v_mul_f32_e32 v32, v70, v30
	v_mov_b32_dpp v28, v31 row_ror:8 row_mask:0xf bank_mask:0xf
	v_fmac_f32_e32 v28, v70, v29
	v_mov_b32_e32 v29, 0
	v_mov_b32_e32 v26, v24
	v_mov_b32_e32 v27, v25
	v_mov_b32_dpp v29, v32 row_ror:8 row_mask:0xf bank_mask:0xf
	v_sub_f32_e32 v32, v62, v175
	v_exp_f32_e32 v33, v32
	v_sub_f32_e32 v32, v63, v175
	v_exp_f32_e32 v34, v32
	v_mov_b32_e32 v32, 0
	v_mul_f32_e32 v35, v70, v33
	v_fmac_f32_e32 v29, v70, v30
	v_mul_f32_e32 v54, v70, v34
	v_mov_b32_dpp v32, v35 row_ror:8 row_mask:0xf bank_mask:0xf
	v_fmac_f32_e32 v32, v70, v33
	v_mov_b32_e32 v33, 0
	v_mov_b32_e32 v30, v28
	v_mov_b32_e32 v31, v29
	v_mov_b32_dpp v33, v54 row_ror:8 row_mask:0xf bank_mask:0xf
	v_sub_f32_e32 v54, v64, v175
	v_exp_f32_e32 v55, v54
	v_sub_f32_e32 v54, v65, v175
	v_exp_f32_e32 v56, v54
	v_mov_b32_e32 v54, 0
	v_mul_f32_e32 v57, v70, v55
	v_fmac_f32_e32 v33, v70, v34
	v_mul_f32_e32 v58, v70, v56
	v_mov_b32_dpp v54, v57 row_ror:8 row_mask:0xf bank_mask:0xf
	v_fmac_f32_e32 v54, v70, v55
	v_mov_b32_e32 v55, 0
	v_mov_b32_e32 v34, v32
	v_mov_b32_e32 v35, v33
; #define LAS __attribute__((address_space(3)))
; __device__ __forceinline__ void attn_unit(const Frame& F, unsigned char* ws, int g, int qt) {
;     ...
;         for (int r = 0; r < 16; ++r) { float v0 = __builtin_amdgcn_exp2f(p0[r] - m_c) * inv_lc, v1 = __builtin_amdgcn_exp2f(p1[r] - m_c) * inv_lc;
;             v0 += __int_as_float(__builtin_amdgcn_update_dpp(0, __float_as_int(v0), 0x128, 0xf, 0xf, false)); v1 += __int_as_float(__builtin_amdgcn_update_dpp(0, __float_as_int(v1), 0x128, 0xf, 0xf, false));
;             { auto q0 = __builtin_amdgcn_permlane16_swap(__float_as_uint(v0), __float_as_uint(v0), false, false); v0 = __uint_as_float(q0[0]) + __uint_as_float(q0[1]); }
;             { auto q1 = __builtin_amdgcn_permlane16_swap(__float_as_uint(v1), __float_as_uint(v1), false, false); v1 = __uint_as_float(q1[0]) + __uint_as_float(q1[1]); }
;             p0[r] = v0; p1[r] = v1; }
;         if (r32 < 8) {
;             LAS float* row = imp + tl * IMP_LD + 16 * i + hi;
; #pragma unroll
;             for (int a4 = 0; a4 < 4; ++a4) {
;                 const float s0 = (p0[4 * a4] + p0[4 * a4 + 1]) + (p0[4 * a4 + 2] + p0[4 * a4 + 3]), s1 = (p1[4 * a4] + p1[4 * a4 + 1]) + (p1[4 * a4 + 2] + p1[4 * a4 + 3]);
;                 atomicAdd((float*)(row + 2 * a4), s0); atomicAdd((float*)(row + 2 * a4 + 8), s1);
;                 atomicAdd((float*)(row + 2 * a4 + 1), p0[4 * a4 + 3]); atomicAdd((float*)(row + 2 * a4 + 9), p1[4 * a4 + 3]); }
;         }
	v_mov_b32_dpp v55, v58 row_ror:8 row_mask:0xf bank_mask:0xf
	v_sub_f32_e32 v58, v66, v175
	v_exp_f32_e32 v59, v58
	v_sub_f32_e32 v58, v67, v175
	v_exp_f32_e32 v60, v58
	v_mov_b32_e32 v58, 0
	v_mul_f32_e32 v61, v70, v59
	v_fmac_f32_e32 v55, v70, v56
	v_mul_f32_e32 v62, v70, v60
	v_mov_b32_dpp v58, v61 row_ror:8 row_mask:0xf bank_mask:0xf
	v_fmac_f32_e32 v58, v70, v59
	v_mov_b32_e32 v59, 0
	v_mov_b32_e32 v56, v54
	v_mov_b32_e32 v57, v55
	v_mov_b32_dpp v59, v62 row_ror:8 row_mask:0xf bank_mask:0xf
	v_sub_f32_e32 v62, v68, v175
	v_exp_f32_e32 v63, v62
	v_sub_f32_e32 v62, v69, v175
	v_exp_f32_e32 v64, v62
	v_mov_b32_e32 v62, 0
	v_mul_f32_e32 v65, v70, v63
	v_fmac_f32_e32 v59, v70, v60
	v_mul_f32_e32 v66, v70, v64
	v_mov_b32_dpp v62, v65 row_ror:8 row_mask:0xf bank_mask:0xf
	v_fmac_f32_e32 v62, v70, v63
	v_mov_b32_e32 v63, 0
	v_mov_b32_e32 v60, v58
	v_mov_b32_e32 v61, v59
	v_mov_b32_dpp v63, v66 row_ror:8 row_mask:0xf bank_mask:0xf
	v_sub_f32_e32 v66, v71, v175
	v_exp_f32_e32 v67, v66
	v_sub_f32_e32 v66, v72, v175
	v_exp_f32_e32 v68, v66
	v_mov_b32_e32 v66, 0
	v_mul_f32_e32 v69, v70, v67
	v_fmac_f32_e32 v63, v70, v64
	v_mul_f32_e32 v71, v70, v68
	v_mov_b32_dpp v66, v69 row_ror:8 row_mask:0xf bank_mask:0xf
	v_fmac_f32_e32 v66, v70, v67
	v_mov_b32_e32 v67, 0
	v_mov_b32_e32 v64, v62
	v_mov_b32_e32 v65, v63
	v_mov_b32_dpp v67, v71 row_ror:8 row_mask:0xf bank_mask:0xf
	v_sub_f32_e32 v71, v73, v175
	v_exp_f32_e32 v72, v71
	v_sub_f32_e32 v71, v74, v175
	v_exp_f32_e32 v73, v71
	v_mov_b32_e32 v71, 0
	v_mul_f32_e32 v74, v70, v72
	v_fmac_f32_e32 v67, v70, v68
	v_mul_f32_e32 v77, v70, v73
	v_mov_b32_dpp v71, v74 row_ror:8 row_mask:0xf bank_mask:0xf
	v_fmac_f32_e32 v71, v70, v72
	v_mov_b32_e32 v72, 0
	v_mov_b32_e32 v68, v66
	v_mov_b32_e32 v69, v67
	v_mov_b32_dpp v72, v77 row_ror:8 row_mask:0xf bank_mask:0xf
	v_exp_f32_e32 v77, v75
	v_sub_f32_e32 v75, v76, v175
	v_exp_f32_e32 v78, v75
	v_mov_b32_e32 v75, 0
	v_mul_f32_e32 v76, v70, v77
	v_fmac_f32_e32 v72, v70, v73
	v_mul_f32_e32 v81, v70, v78
	v_mov_b32_dpp v75, v76 row_ror:8 row_mask:0xf bank_mask:0xf
	v_mov_b32_e32 v76, 0
	v_fmac_f32_e32 v75, v70, v77
	v_mov_b32_e32 v73, v71
	v_mov_b32_dpp v76, v81 row_ror:8 row_mask:0xf bank_mask:0xf
	v_exp_f32_e32 v81, v79
	v_sub_f32_e32 v79, v80, v175
	v_exp_f32_e32 v82, v79
	v_mov_b32_e32 v79, 0
	v_mul_f32_e32 v80, v70, v81
	v_fmac_f32_e32 v76, v70, v78
	v_mul_f32_e32 v85, v70, v82
	v_mov_b32_dpp v79, v80 row_ror:8 row_mask:0xf bank_mask:0xf
	v_mov_b32_e32 v80, 0
	v_fmac_f32_e32 v79, v70, v81
	v_mov_b32_e32 v74, v72
	v_mov_b32_dpp v80, v85 row_ror:8 row_mask:0xf bank_mask:0xf
	v_exp_f32_e32 v85, v83
	v_sub_f32_e32 v83, v84, v175
	v_exp_f32_e32 v86, v83
	v_mov_b32_e32 v83, 0
	v_mul_f32_e32 v84, v70, v85
	v_fmac_f32_e32 v80, v70, v82
	v_mul_f32_e32 v87, v70, v86
	v_mov_b32_dpp v83, v84 row_ror:8 row_mask:0xf bank_mask:0xf
	v_mov_b32_e32 v84, 0
	v_fmac_f32_e32 v83, v70, v85
	v_mov_b32_e32 v77, v75
	v_mov_b32_dpp v84, v87 row_ror:8 row_mask:0xf bank_mask:0xf
	v_fmac_f32_e32 v84, v70, v86
	v_mov_b32_e32 v78, v76
	v_mov_b32_e32 v81, v79
	v_mov_b32_e32 v82, v80
	v_mov_b32_e32 v85, v83
	v_mov_b32_e32 v86, v84
	v_permlane16_swap_b32_e32 v8, v10
	v_permlane16_swap_b32_e32 v9, v11
	v_permlane16_swap_b32_e32 v12, v14
	v_permlane16_swap_b32_e32 v13, v15
	v_permlane16_swap_b32_e32 v16, v18
	v_permlane16_swap_b32_e32 v17, v19
	v_permlane16_swap_b32_e32 v20, v22
	v_permlane16_swap_b32_e32 v21, v23
	v_permlane16_swap_b32_e32 v24, v26
	v_permlane16_swap_b32_e32 v25, v27
	v_permlane16_swap_b32_e32 v28, v30
	v_permlane16_swap_b32_e32 v29, v31
	v_permlane16_swap_b32_e32 v32, v34
	v_permlane16_swap_b32_e32 v33, v35
	v_permlane16_swap_b32_e32 v54, v56
	v_permlane16_swap_b32_e32 v55, v57
	v_permlane16_swap_b32_e32 v58, v60
	v_permlane16_swap_b32_e32 v59, v61
	v_permlane16_swap_b32_e32 v62, v64
	v_permlane16_swap_b32_e32 v63, v65
	v_permlane16_swap_b32_e32 v66, v68
	v_permlane16_swap_b32_e32 v67, v69
	v_permlane16_swap_b32_e32 v71, v73
	v_permlane16_swap_b32_e32 v72, v74
	v_permlane16_swap_b32_e32 v75, v77
	v_permlane16_swap_b32_e32 v76, v78
	v_permlane16_swap_b32_e32 v79, v81
	v_permlane16_swap_b32_e32 v80, v82
	v_permlane16_swap_b32_e32 v83, v85
	v_permlane16_swap_b32_e32 v84, v86
	s_and_saveexec_b64 s[10:11], vcc
	s_cbranch_execz .LBB0_626
	v_add_f32_e32 v16, v16, v18
	v_add_f32_e32 v12, v12, v14
	v_add_f32_e32 v8, v8, v10
	v_add_f32_e32 v4, v4, v6
	v_add_f32_e32 v17, v17, v19
	v_add_f32_e32 v13, v13, v15
	v_add_f32_e32 v9, v9, v11
	v_add_f32_e32 v5, v5, v7
	v_add_f32_e32 v4, v4, v8
	v_add_f32_e32 v6, v12, v16
	v_add_f32_e32 v4, v4, v6
	v_add_f32_e32 v5, v5, v9
	v_add_f32_e32 v6, v13, v17
	v_add_f32_e32 v32, v32, v34
	v_add_f32_e32 v28, v28, v30
	v_add_f32_e32 v24, v24, v26
	v_add_f32_e32 v20, v20, v22
	v_add_f32_e32 v5, v5, v6
	v_add_f32_e32 v33, v33, v35
	v_add_f32_e32 v29, v29, v31
	v_add_f32_e32 v25, v25, v27
	v_add_f32_e32 v21, v21, v23
	s_waitcnt vmcnt(0)
	ds_add_f32 v53, v4
	ds_add_f32 v53, v5 offset:32
	ds_add_f32 v53, v16 offset:4
	ds_add_f32 v53, v17 offset:36
	v_add_f32_e32 v4, v20, v24
	v_add_f32_e32 v5, v28, v32
	v_add_f32_e32 v4, v4, v5
	v_add_f32_e32 v5, v21, v25
	v_add_f32_e32 v6, v29, v33
	v_add_f32_e32 v66, v66, v68
	v_add_f32_e32 v62, v62, v64
	v_add_f32_e32 v58, v58, v60
	v_add_f32_e32 v54, v54, v56
	v_add_f32_e32 v5, v5, v6
	v_add_f32_e32 v67, v67, v69
	v_add_f32_e32 v63, v63, v65
	v_add_f32_e32 v59, v59, v61
	v_add_f32_e32 v55, v55, v57
	ds_add_f32 v53, v4 offset:8
	ds_add_f32 v53, v5 offset:40
	ds_add_f32 v53, v32 offset:12
	ds_add_f32 v53, v33 offset:44
	v_add_f32_e32 v4, v54, v58
	v_add_f32_e32 v5, v62, v66
	v_add_f32_e32 v4, v4, v5
	v_add_f32_e32 v5, v55, v59
	v_add_f32_e32 v6, v63, v67
	v_add_f32_e32 v83, v83, v85
	v_add_f32_e32 v79, v79, v81
	v_add_f32_e32 v75, v75, v77
	v_add_f32_e32 v71, v71, v73
	v_add_f32_e32 v5, v5, v6
	v_add_f32_e32 v84, v84, v86
	v_add_f32_e32 v80, v80, v82
	v_add_f32_e32 v76, v76, v78
	v_add_f32_e32 v72, v72, v74
	ds_add_f32 v53, v4 offset:16
	ds_add_f32 v53, v5 offset:48
	ds_add_f32 v53, v66 offset:20
	ds_add_f32 v53, v67 offset:52
	v_add_f32_e32 v4, v71, v75
	v_add_f32_e32 v5, v79, v83
	v_add_f32_e32 v4, v4, v5
	v_add_f32_e32 v5, v72, v76
	v_add_f32_e32 v6, v80, v84
	v_add_f32_e32 v5, v5, v6
	ds_add_f32 v53, v4 offset:24
	ds_add_f32 v53, v5 offset:56
	ds_add_f32 v53, v83 offset:28
	ds_add_f32 v53, v84 offset:60
	s_branch .LBB0_626

; #define LAS __attribute__((address_space(3)))
; #define SBAR() __builtin_amdgcn_sched_barrier(0)
; template <int OFF> __device__ __forceinline__ s16x4 tr_read(int vb) { s16x4 r; asm volatile("ds_read_b64_tr_b16 %0, %1 offset:%2" : "=&v"(r) : "v"(vb), "i"(OFF) : "memory"); return r; }
; __device__ __forceinline__ void qkt(f32x16& p0, f32x16& p1, const LAS char* Ks, const bf16x8 (&qr)[8], int r32, int hi) {
;     p0 = f32x16{}; p1 = f32x16{};
; #pragma unroll
;     for (int d0 = 0; d0 < 8; ++d0) { const int cb = (d0 * 16 + hi * 8) * 2;
;         const bf16x8 b0 = *(const LAS bf16x8*)(Ks + KSWZ(r32, cb));
;         const bf16x8 b1 = *(const LAS bf16x8*)(Ks + KSWZ(32 + r32, cb));
;         p0 = __builtin_amdgcn_mfma_f32_32x32x16_bf16(b0, qr[d0], p0, 0, 0, 0);
;         p1 = __builtin_amdgcn_mfma_f32_32x32x16_bf16(b1, qr[d0], p1, 0, 0, 0);
;         if (d0 == 3) SBAR(); }
; }
; template <int D0> __device__ __forceinline__ void pv_one(f32x16& od, int vb, bf16x8 pa0, bf16x8 pa1, bf16x8 pa2, bf16x8 pa3) {
;     const s16x4 l0 = tr_read<v_rd_off(D0, 0, 0)>(vb), h0 = tr_read<v_rd_off(D0, 0, 1)>(vb), l1 = tr_read<v_rd_off(D0, 1, 0)>(vb), h1 = tr_read<v_rd_off(D0, 1, 1)>(vb);
;     const s16x4 l2 = tr_read<v_rd_off(D0, 2, 0)>(vb), h2 = tr_read<v_rd_off(D0, 2, 1)>(vb), l3 = tr_read<v_rd_off(D0, 3, 0)>(vb), h3 = tr_read<v_rd_off(D0, 3, 1)>(vb);
;     asm volatile("s_waitcnt lgkmcnt(0)" ::: "memory"); SBAR();
;     ...
;     od = __builtin_amdgcn_mfma_f32_32x32x16_bf16(pa0, PK(l0, h0), od, 0, 0, 0);
;     od = __builtin_amdgcn_mfma_f32_32x32x16_bf16(pa1, PK(l1, h1), od, 0, 0, 0);
;     od = __builtin_amdgcn_mfma_f32_32x32x16_bf16(pa2, PK(l2, h2), od, 0, 0, 0);
;     od = __builtin_amdgcn_mfma_f32_32x32x16_bf16(pa3, PK(l3, h3), od, 0, 0, 0);
;     ...
; }
.LBB0_755:
	s_barrier
	v_add_f32_e32 v2, v2, v20
	v_add_f32_e32 v2, v52, v2
	s_andn2_b64 vcc, exec, s[10:11]
	s_mov_b32 s16, 1
	s_cbranch_vccnz .LBB0_766
	v_readlane_b32 s10, v245, 40
	v_add_u32_e32 v183, 0xc000, v173
	s_nop 0
	v_mov_b32_e32 v20, s10
	ds_read_b32 v20, v20
	ds_read_b64_tr_b16 v[36:37], v165 offset:0
	ds_read_b64_tr_b16 v[38:39], v165 offset:0x800
	ds_read_b64_tr_b16 v[40:41], v165 offset:0x1000
	ds_read_b64_tr_b16 v[42:43], v165 offset:0x1800
	ds_read_b64_tr_b16 v[44:45], v165 offset:0x2000
	ds_read_b64_tr_b16 v[46:47], v165 offset:0x2800
	ds_read_b64_tr_b16 v[48:49], v165 offset:0x3000
	ds_read_b64_tr_b16 v[50:51], v165 offset:0x3800
	s_waitcnt lgkmcnt(0)
	s_waitcnt lgkmcnt(0)
	v_readfirstlane_b32 s16, v20
	v_mfma_f32_32x32x16_bf16 v[20:35], v[72:75], v[36:39], v[4:19]
	v_add_u32_e32 v247, v183, v174
	ds_read_b128 v[212:215], v247 offset:16384
	ds_read_b64_tr_b16 v[52:53], v165 offset:0x200
	ds_read_b64_tr_b16 v[54:55], v165 offset:0xa00
	ds_read_b64_tr_b16 v[56:57], v165 offset:0x1200
	ds_read_b64_tr_b16 v[58:59], v165 offset:0x1a00
	ds_read_b64_tr_b16 v[60:61], v165 offset:0x2200
	ds_read_b64_tr_b16 v[62:63], v165 offset:0x2a00
	ds_read_b64_tr_b16 v[64:65], v165 offset:0x3200
	v_mfma_f32_32x32x16_bf16 v[20:35], v[76:79], v[40:43], v[20:35]
	ds_read_b128 v[216:219], v247 offset:24576
	ds_read_b64_tr_b16 v[66:67], v165 offset:0x3a00
	s_waitcnt lgkmcnt(0)
	v_mfma_f32_32x32x16_bf16 v[20:35], v[80:83], v[44:47], v[20:35]
	v_add_u32_e32 v247, v183, v175
	ds_read_b128 v[220:223], v247 offset:16384
	v_mfma_f32_32x32x16_bf16 v[20:35], v[68:71], v[48:51], v[20:35]
	ds_read_b128 v[224:227], v247 offset:24576
	v_mfma_f32_32x32x16_bf16 v[36:51], v[72:75], v[52:55], v[4:19]
	v_add_u32_e32 v247, v183, v176
	ds_read_b128 v[228:231], v247 offset:16384
	ds_read_b64_tr_b16 v[84:85], v165 offset:0x400
	ds_read_b64_tr_b16 v[86:87], v165 offset:0xc00
	ds_read_b64_tr_b16 v[88:89], v165 offset:0x1400
	ds_read_b64_tr_b16 v[90:91], v165 offset:0x1c00
	ds_read_b64_tr_b16 v[92:93], v165 offset:0x2400
	ds_read_b64_tr_b16 v[94:95], v165 offset:0x2c00
	ds_read_b64_tr_b16 v[96:97], v165 offset:0x3400
	v_mfma_f32_32x32x16_bf16 v[36:51], v[76:79], v[56:59], v[36:51]
	ds_read_b128 v[232:235], v247 offset:24576
	ds_read_b64_tr_b16 v[98:99], v165 offset:0x3c00
	s_waitcnt lgkmcnt(0)
	v_mfma_f32_32x32x16_bf16 v[36:51], v[80:83], v[60:63], v[36:51]
	v_add_u32_e32 v247, v183, v177
	ds_read_b128 v[236:239], v247 offset:16384
	v_mfma_f32_32x32x16_bf16 v[36:51], v[68:71], v[64:67], v[36:51]
	ds_read_b128 v[240:243], v247 offset:24576
	v_mfma_f32_32x32x16_bf16 v[52:67], v[72:75], v[84:87], v[4:19]
	ds_read_b64_tr_b16 v[84:85], v165 offset:0x600
	ds_read_b64_tr_b16 v[86:87], v165 offset:0xe00
	v_mfma_f32_32x32x16_bf16 v[52:67], v[76:79], v[88:91], v[52:67]
	ds_read_b64_tr_b16 v[88:89], v165 offset:0x1600
	ds_read_b64_tr_b16 v[90:91], v165 offset:0x1e00
	v_mfma_f32_32x32x16_bf16 v[52:67], v[80:83], v[92:95], v[52:67]
	ds_read_b64_tr_b16 v[92:93], v165 offset:0x2600
	ds_read_b64_tr_b16 v[94:95], v165 offset:0x2e00
	v_mfma_f32_32x32x16_bf16 v[52:67], v[68:71], v[96:99], v[52:67]
	ds_read_b64_tr_b16 v[96:97], v165 offset:0x3600
	ds_read_b64_tr_b16 v[98:99], v165 offset:0x3e00
	s_waitcnt lgkmcnt(0)
	v_mfma_f32_32x32x16_bf16 v[4:19], v[72:75], v[84:87], v[4:19]
	v_mfma_f32_32x32x16_bf16 v[4:19], v[76:79], v[88:91], v[4:19]
	v_mfma_f32_32x32x16_bf16 v[4:19], v[80:83], v[92:95], v[4:19]
	v_mfma_f32_32x32x16_bf16 v[4:19], v[68:71], v[96:99], v[4:19]
	v_mfma_f32_32x32x16_bf16 v[68:83], v[212:215], v[124:127], 0
	v_add_u32_e32 v247, v183, v178
	ds_read_b128 v[212:215], v247 offset:16384
	v_mfma_f32_32x32x16_bf16 v[84:99], v[216:219], v[124:127], 0
	ds_read_b128 v[216:219], v247 offset:24576
	v_mfma_f32_32x32x16_bf16 v[68:83], v[220:223], v[100:103], v[68:83]
	v_add_u32_e32 v247, v183, v179
	ds_read_b128 v[220:223], v247 offset:16384
	v_mfma_f32_32x32x16_bf16 v[84:99], v[224:227], v[100:103], v[84:99]
	ds_read_b128 v[224:227], v247 offset:24576
	v_mfma_f32_32x32x16_bf16 v[68:83], v[228:231], v[104:107], v[68:83]
	v_add_u32_e32 v247, v183, v180
	ds_read_b128 v[228:231], v247 offset:16384
	v_mfma_f32_32x32x16_bf16 v[84:99], v[232:235], v[104:107], v[84:99]
	ds_read_b128 v[232:235], v247 offset:24576
	v_mfma_f32_32x32x16_bf16 v[68:83], v[236:239], v[108:111], v[68:83]
	v_add_u32_e32 v247, v183, v181
	ds_read_b128 v[236:239], v247 offset:16384
	v_mfma_f32_32x32x16_bf16 v[84:99], v[240:243], v[108:111], v[84:99]
	ds_read_b128 v[240:243], v247 offset:24576
	s_waitcnt lgkmcnt(7)
	v_mfma_f32_32x32x16_bf16 v[68:83], v[212:215], v[112:115], v[68:83]
	s_waitcnt lgkmcnt(6)
	v_mfma_f32_32x32x16_bf16 v[84:99], v[216:219], v[112:115], v[84:99]
	s_waitcnt lgkmcnt(5)
	v_mfma_f32_32x32x16_bf16 v[68:83], v[220:223], v[116:119], v[68:83]
	s_waitcnt lgkmcnt(4)
	v_mfma_f32_32x32x16_bf16 v[84:99], v[224:227], v[116:119], v[84:99]
	s_waitcnt lgkmcnt(3)
	v_mfma_f32_32x32x16_bf16 v[68:83], v[228:231], v[120:123], v[68:83]
	s_waitcnt lgkmcnt(2)
	v_mfma_f32_32x32x16_bf16 v[84:99], v[232:235], v[120:123], v[84:99]
	s_waitcnt lgkmcnt(1)
	v_mfma_f32_32x32x16_bf16 v[68:83], v[236:239], v[128:131], v[68:83]
	s_waitcnt lgkmcnt(0)
	s_andn2_b64 vcc, exec, s[12:13]
	v_cndmask_b32_e64 v183, 0, 1, s[12:13]
	v_cmp_ne_u32_e64 s[10:11], 1, v183
	v_mfma_f32_32x32x16_bf16 v[84:99], v[240:243], v[128:131], v[84:99]
	s_cbranch_vccnz .LBB0_758
	s_waitcnt vmcnt(0)

; #define LAS __attribute__((address_space(3)))
; #define SBAR() __builtin_amdgcn_sched_barrier(0)
; template <int OFF> __device__ __forceinline__ s16x4 tr_read(int vb) { s16x4 r; asm volatile("ds_read_b64_tr_b16 %0, %1 offset:%2" : "=&v"(r) : "v"(vb), "i"(OFF) : "memory"); return r; }
; __device__ __forceinline__ void qkt(f32x16& p0, f32x16& p1, const LAS char* Ks, const bf16x8 (&qr)[8], int r32, int hi) {
;     p0 = f32x16{}; p1 = f32x16{};
; #pragma unroll
;     for (int d0 = 0; d0 < 8; ++d0) { const int cb = (d0 * 16 + hi * 8) * 2;
;         const bf16x8 b0 = *(const LAS bf16x8*)(Ks + KSWZ(r32, cb));
;         const bf16x8 b1 = *(const LAS bf16x8*)(Ks + KSWZ(32 + r32, cb));
;         p0 = __builtin_amdgcn_mfma_f32_32x32x16_bf16(b0, qr[d0], p0, 0, 0, 0);
;         p1 = __builtin_amdgcn_mfma_f32_32x32x16_bf16(b1, qr[d0], p1, 0, 0, 0);
;         if (d0 == 3) SBAR(); }
; }
; template <int D0> __device__ __forceinline__ void pv_one(f32x16& od, int vb, bf16x8 pa0, bf16x8 pa1, bf16x8 pa2, bf16x8 pa3) {
;     const s16x4 l0 = tr_read<v_rd_off(D0, 0, 0)>(vb), h0 = tr_read<v_rd_off(D0, 0, 1)>(vb), l1 = tr_read<v_rd_off(D0, 1, 0)>(vb), h1 = tr_read<v_rd_off(D0, 1, 1)>(vb);
;     const s16x4 l2 = tr_read<v_rd_off(D0, 2, 0)>(vb), h2 = tr_read<v_rd_off(D0, 2, 1)>(vb), l3 = tr_read<v_rd_off(D0, 3, 0)>(vb), h3 = tr_read<v_rd_off(D0, 3, 1)>(vb);
;     asm volatile("s_waitcnt lgkmcnt(0)" ::: "memory"); SBAR();
;     ...
;     od = __builtin_amdgcn_mfma_f32_32x32x16_bf16(pa0, PK(l0, h0), od, 0, 0, 0);
;     od = __builtin_amdgcn_mfma_f32_32x32x16_bf16(pa1, PK(l1, h1), od, 0, 0, 0);
;     od = __builtin_amdgcn_mfma_f32_32x32x16_bf16(pa2, PK(l2, h2), od, 0, 0, 0);
;     od = __builtin_amdgcn_mfma_f32_32x32x16_bf16(pa3, PK(l3, h3), od, 0, 0, 0);
;     ...
; }
.LBB0_813:
	s_barrier
	v_add_f32_e32 v2, v2, v21
	v_add_f32_e32 v179, v20, v2
	s_andn2_b64 vcc, exec, s[64:65]
	s_mov_b32 s96, 1
	s_cbranch_vccnz .LBB0_824
	s_add_i32 s10, 0, 0x21064
	v_mov_b32_e32 v2, s10
	ds_read_b32 v2, v2
	ds_read_b64_tr_b16 v[36:37], v165 offset:0
	ds_read_b64_tr_b16 v[38:39], v165 offset:0x800
	ds_read_b64_tr_b16 v[40:41], v165 offset:0x1000
	ds_read_b64_tr_b16 v[42:43], v165 offset:0x1800
	ds_read_b64_tr_b16 v[44:45], v165 offset:0x2000
	ds_read_b64_tr_b16 v[46:47], v165 offset:0x2800
	ds_read_b64_tr_b16 v[48:49], v165 offset:0x3000
	ds_read_b64_tr_b16 v[50:51], v165 offset:0x3800
	s_waitcnt lgkmcnt(0)
	s_waitcnt lgkmcnt(0)
	v_readfirstlane_b32 s12, v2
	v_add_u32_e32 v184, 0xc000, v170
	v_mfma_f32_32x32x16_bf16 v[20:35], v[72:75], v[36:39], v[4:19]
	v_add_u32_e32 v247, v184, v171
	ds_read_b128 v[212:215], v247 offset:16384
	ds_read_b64_tr_b16 v[52:53], v165 offset:0x200
	ds_read_b64_tr_b16 v[54:55], v165 offset:0xa00
	ds_read_b64_tr_b16 v[56:57], v165 offset:0x1200
	ds_read_b64_tr_b16 v[58:59], v165 offset:0x1a00
	ds_read_b64_tr_b16 v[60:61], v165 offset:0x2200
	ds_read_b64_tr_b16 v[62:63], v165 offset:0x2a00
	ds_read_b64_tr_b16 v[64:65], v165 offset:0x3200
	v_mfma_f32_32x32x16_bf16 v[20:35], v[76:79], v[40:43], v[20:35]
	ds_read_b128 v[216:219], v247 offset:24576
	ds_read_b64_tr_b16 v[66:67], v165 offset:0x3a00
	s_waitcnt lgkmcnt(0)
	v_mfma_f32_32x32x16_bf16 v[20:35], v[80:83], v[44:47], v[20:35]
	v_add_u32_e32 v247, v184, v172
	ds_read_b128 v[220:223], v247 offset:16384
	v_mfma_f32_32x32x16_bf16 v[20:35], v[68:71], v[48:51], v[20:35]
	ds_read_b128 v[224:227], v247 offset:24576
	v_mfma_f32_32x32x16_bf16 v[36:51], v[72:75], v[52:55], v[4:19]
	v_add_u32_e32 v247, v184, v173
	ds_read_b128 v[228:231], v247 offset:16384
	ds_read_b64_tr_b16 v[84:85], v165 offset:0x400
	ds_read_b64_tr_b16 v[86:87], v165 offset:0xc00
	ds_read_b64_tr_b16 v[88:89], v165 offset:0x1400
	ds_read_b64_tr_b16 v[90:91], v165 offset:0x1c00
	ds_read_b64_tr_b16 v[92:93], v165 offset:0x2400
	ds_read_b64_tr_b16 v[94:95], v165 offset:0x2c00
	ds_read_b64_tr_b16 v[96:97], v165 offset:0x3400
	v_mfma_f32_32x32x16_bf16 v[36:51], v[76:79], v[56:59], v[36:51]
	ds_read_b128 v[232:235], v247 offset:24576
	ds_read_b64_tr_b16 v[98:99], v165 offset:0x3c00
	s_waitcnt lgkmcnt(0)
	v_mfma_f32_32x32x16_bf16 v[36:51], v[80:83], v[60:63], v[36:51]
	v_add_u32_e32 v247, v184, v174
	ds_read_b128 v[236:239], v247 offset:16384
	v_mfma_f32_32x32x16_bf16 v[36:51], v[68:71], v[64:67], v[36:51]
	ds_read_b128 v[240:243], v247 offset:24576
	v_mfma_f32_32x32x16_bf16 v[52:67], v[72:75], v[84:87], v[4:19]
	ds_read_b64_tr_b16 v[84:85], v165 offset:0x600
	ds_read_b64_tr_b16 v[86:87], v165 offset:0xe00
	v_mfma_f32_32x32x16_bf16 v[52:67], v[76:79], v[88:91], v[52:67]
	ds_read_b64_tr_b16 v[88:89], v165 offset:0x1600
	ds_read_b64_tr_b16 v[90:91], v165 offset:0x1e00
	v_mfma_f32_32x32x16_bf16 v[52:67], v[80:83], v[92:95], v[52:67]
	ds_read_b64_tr_b16 v[92:93], v165 offset:0x2600
	ds_read_b64_tr_b16 v[94:95], v165 offset:0x2e00
	v_mfma_f32_32x32x16_bf16 v[52:67], v[68:71], v[96:99], v[52:67]
	ds_read_b64_tr_b16 v[96:97], v165 offset:0x3600
	ds_read_b64_tr_b16 v[98:99], v165 offset:0x3e00
	s_waitcnt lgkmcnt(0)
	v_mfma_f32_32x32x16_bf16 v[4:19], v[72:75], v[84:87], v[4:19]
	v_mfma_f32_32x32x16_bf16 v[4:19], v[76:79], v[88:91], v[4:19]
	v_mfma_f32_32x32x16_bf16 v[4:19], v[80:83], v[92:95], v[4:19]
	v_mfma_f32_32x32x16_bf16 v[4:19], v[68:71], v[96:99], v[4:19]
	v_mfma_f32_32x32x16_bf16 v[68:83], v[212:215], v[124:127], 0
	v_add_u32_e32 v247, v184, v175
	ds_read_b128 v[212:215], v247 offset:16384
	v_mfma_f32_32x32x16_bf16 v[84:99], v[216:219], v[124:127], 0
	ds_read_b128 v[216:219], v247 offset:24576
	v_mfma_f32_32x32x16_bf16 v[68:83], v[220:223], v[100:103], v[68:83]
	v_add_u32_e32 v247, v184, v176
	ds_read_b128 v[220:223], v247 offset:16384
	v_mfma_f32_32x32x16_bf16 v[84:99], v[224:227], v[100:103], v[84:99]
	ds_read_b128 v[224:227], v247 offset:24576
	v_mfma_f32_32x32x16_bf16 v[68:83], v[228:231], v[104:107], v[68:83]
	v_add_u32_e32 v247, v184, v177
	ds_read_b128 v[228:231], v247 offset:16384
	v_mfma_f32_32x32x16_bf16 v[84:99], v[232:235], v[104:107], v[84:99]
	ds_read_b128 v[232:235], v247 offset:24576
	v_mfma_f32_32x32x16_bf16 v[68:83], v[236:239], v[108:111], v[68:83]
	v_add_u32_e32 v247, v184, v178
	ds_read_b128 v[236:239], v247 offset:16384
	v_mfma_f32_32x32x16_bf16 v[84:99], v[240:243], v[108:111], v[84:99]
	ds_read_b128 v[240:243], v247 offset:24576
	s_waitcnt lgkmcnt(7)
	v_mfma_f32_32x32x16_bf16 v[68:83], v[212:215], v[112:115], v[68:83]
	s_waitcnt lgkmcnt(6)
	v_mfma_f32_32x32x16_bf16 v[84:99], v[216:219], v[112:115], v[84:99]
	s_waitcnt lgkmcnt(5)
	v_mfma_f32_32x32x16_bf16 v[68:83], v[220:223], v[116:119], v[68:83]
	s_waitcnt lgkmcnt(4)
	v_mfma_f32_32x32x16_bf16 v[84:99], v[224:227], v[116:119], v[84:99]
	s_waitcnt lgkmcnt(3)
	v_mfma_f32_32x32x16_bf16 v[68:83], v[228:231], v[120:123], v[68:83]
	s_waitcnt lgkmcnt(2)
	v_mfma_f32_32x32x16_bf16 v[84:99], v[232:235], v[120:123], v[84:99]
	s_waitcnt lgkmcnt(1)
	v_mfma_f32_32x32x16_bf16 v[68:83], v[236:239], v[128:131], v[68:83]
	s_waitcnt lgkmcnt(0)
	s_mov_b32 s64, 0
	s_andn2_b64 vcc, exec, s[62:63]
	s_mov_b32 s65, 0x41800000
	v_cndmask_b32_e64 v2, 0, 1, s[62:63]
	v_cmp_ne_u32_e64 s[10:11], 1, v2
	v_mfma_f32_32x32x16_bf16 v[84:99], v[240:243], v[128:131], v[84:99]
	s_cbranch_vccnz .LBB0_816
	s_waitcnt vmcnt(0)
